# speedup vs baseline: 1.0280x; 1.0147x over previous
_Z8gemm_f16ILi128ELi64ELi2ELi2ELi4ELi2ELi0EEvPKDF16_S1_Pviiii:
	s_load_dwordx4 s[4:7], s[0:1], 0x0
	s_load_dwordx2 s[8:9], s[0:1], 0x10
	s_and_b32 s3, s2, 7
	s_lshr_b32 s10, s2, 3
	s_lshr_b32 s11, s3, 1
	s_lshl_b32 s11, s11, 2
	s_and_b32 s12, s10, 3
	s_and_b32 s3, s3, 1
	s_lshl_b32 s3, s3, 3
	s_lshr_b32 s10, s10, 2
	s_add_i32 s10, s10, s3
	s_add_i32 s3, s11, s12
	s_mov_b32 s11, s10
	s_lshl_b32 s10, s3, 7
	s_lshl_b32 s11, s11, 6
	v_lshrrev_b32_e32 v13, 3, v0
	v_and_b32_e32 v14, 7, v0
	v_bfe_u32 v15, v0, 4, 3
	v_xor_b32_e32 v14, v14, v15
	v_lshlrev_b32_e32 v14, 4, v14
	v_add_u32_e32 v15, s10, v13
	v_mul_u32_u24_e32 v15, 0xc00, v15
	v_add_u32_e32 v3, v15, v14
	v_add_u32_e32 v4, 0x18000, v3
	v_add_u32_e32 v5, 0x30000, v3
	v_add_u32_e32 v6, 0x48000, v3
	v_add_u32_e32 v15, s11, v13
	v_mul_u32_u24_e32 v15, 0xc00, v15
	v_add_u32_e32 v7, v15, v14
	v_add_u32_e32 v8, 0x18000, v7
	v_lshlrev_b32_e32 v13, 4, v0
	s_nop 0
	v_readfirstlane_b32 s20, v13
	v_and_b32_e32 v13, 15, v0
	v_bfe_u32 v14, v0, 4, 2
	v_bfe_u32 v15, v0, 1, 3
	v_xor_b32_e32 v14, v14, v15
	v_lshlrev_b32_e32 v14, 4, v14
	v_lshl_or_b32 v14, v13, 7, v14
	v_lshrrev_b32_e32 v13, 7, v0
	v_lshl_or_b32 v1, v13, 13, v14
	v_bfe_u32 v13, v0, 6, 1
	v_lshlrev_b32_e32 v13, 12, v13
	v_or_b32_e32 v13, 0x4000, v13
	v_or_b32_e32 v2, v13, v14
	s_waitcnt lgkmcnt(0)
	s_mov_b32 s14, s4
	s_mov_b32 s15, s5
	s_mov_b32 s16, s6
	s_mov_b32 s17, s7
	s_mov_b32 s21, s20
	s_mov_b32 m0, s21
	s_add_i32 s21, s21, 0x1000
	global_load_lds_dwordx4 v3, s[14:15]
	s_mov_b32 m0, s21
	s_add_i32 s21, s21, 0x1000
	global_load_lds_dwordx4 v4, s[14:15]
	s_mov_b32 m0, s21
	s_add_i32 s21, s21, 0x1000
	global_load_lds_dwordx4 v5, s[14:15]
	s_mov_b32 m0, s21
	s_add_i32 s21, s21, 0x1000
	global_load_lds_dwordx4 v6, s[14:15]
	s_mov_b32 m0, s21
	s_add_i32 s21, s21, 0x1000
	global_load_lds_dwordx4 v7, s[16:17]
	s_mov_b32 m0, s21
	s_add_i32 s21, s21, 0x1000
	global_load_lds_dwordx4 v8, s[16:17]
	s_add_u32 s14, s14, 0x80
	s_addc_u32 s15, s15, 0
	s_add_u32 s16, s16, 0x80
	s_addc_u32 s17, s17, 0
	s_mov_b32 m0, s21
	s_add_i32 s21, s21, 0x1000
	global_load_lds_dwordx4 v3, s[14:15]
	s_mov_b32 m0, s21
	s_add_i32 s21, s21, 0x1000
	global_load_lds_dwordx4 v4, s[14:15]
	s_mov_b32 m0, s21
	s_add_i32 s21, s21, 0x1000
	global_load_lds_dwordx4 v5, s[14:15]
	s_mov_b32 m0, s21
	s_add_i32 s21, s21, 0x1000
	global_load_lds_dwordx4 v6, s[14:15]
	s_mov_b32 m0, s21
	s_add_i32 s21, s21, 0x1000
	global_load_lds_dwordx4 v7, s[16:17]
	s_mov_b32 m0, s21
	s_add_i32 s21, s21, 0x1000
	global_load_lds_dwordx4 v8, s[16:17]
	s_add_u32 s14, s14, 0x80
	s_addc_u32 s15, s15, 0
	s_add_u32 s16, s16, 0x80
	s_addc_u32 s17, s17, 0
	s_mov_b32 m0, s21
	s_add_i32 s21, s21, 0x1000
	global_load_lds_dwordx4 v3, s[14:15]
	s_mov_b32 m0, s21
	s_add_i32 s21, s21, 0x1000
	global_load_lds_dwordx4 v4, s[14:15]
	s_mov_b32 m0, s21
	s_add_i32 s21, s21, 0x1000
	global_load_lds_dwordx4 v5, s[14:15]
	s_mov_b32 m0, s21
	s_add_i32 s21, s21, 0x1000
	global_load_lds_dwordx4 v6, s[14:15]
	s_mov_b32 m0, s21
	s_add_i32 s21, s21, 0x1000
	global_load_lds_dwordx4 v7, s[16:17]
	s_mov_b32 m0, s21
	s_add_i32 s21, s21, 0x1000
	global_load_lds_dwordx4 v8, s[16:17]
	s_add_u32 s14, s14, 0x80
	s_addc_u32 s15, s15, 0
	s_add_u32 s16, s16, 0x80
	s_addc_u32 s17, s17, 0
	s_mov_b32 m0, s21
	s_add_i32 s21, s21, 0x1000
	global_load_lds_dwordx4 v3, s[14:15]
	s_mov_b32 m0, s21
	s_add_i32 s21, s21, 0x1000
	global_load_lds_dwordx4 v4, s[14:15]
	s_mov_b32 m0, s21
	s_add_i32 s21, s21, 0x1000
	global_load_lds_dwordx4 v5, s[14:15]
	s_mov_b32 m0, s21
	s_add_i32 s21, s21, 0x1000
	global_load_lds_dwordx4 v6, s[14:15]
	s_mov_b32 m0, s21
	s_add_i32 s21, s21, 0x1000
	global_load_lds_dwordx4 v7, s[16:17]
	s_mov_b32 m0, s21
	s_add_i32 s21, s21, 0x1000
	global_load_lds_dwordx4 v8, s[16:17]
	v_accvgpr_write_b32 a0, 0
	v_accvgpr_write_b32 a1, 0
	v_accvgpr_write_b32 a2, 0
	v_accvgpr_write_b32 a3, 0
	v_accvgpr_write_b32 a4, 0
	v_accvgpr_write_b32 a5, 0
	v_accvgpr_write_b32 a6, 0
	v_accvgpr_write_b32 a7, 0
	v_accvgpr_write_b32 a8, 0
	v_accvgpr_write_b32 a9, 0
	v_accvgpr_write_b32 a10, 0
	v_accvgpr_write_b32 a11, 0
	v_accvgpr_write_b32 a12, 0
	v_accvgpr_write_b32 a13, 0
	v_accvgpr_write_b32 a14, 0
	v_accvgpr_write_b32 a15, 0
	v_accvgpr_write_b32 a16, 0
	v_accvgpr_write_b32 a17, 0
	v_accvgpr_write_b32 a18, 0
	v_accvgpr_write_b32 a19, 0
	v_accvgpr_write_b32 a20, 0
	v_accvgpr_write_b32 a21, 0
	v_accvgpr_write_b32 a22, 0
	v_accvgpr_write_b32 a23, 0
	v_accvgpr_write_b32 a24, 0
	v_accvgpr_write_b32 a25, 0
	v_accvgpr_write_b32 a26, 0
	v_accvgpr_write_b32 a27, 0
	v_accvgpr_write_b32 a28, 0
	v_accvgpr_write_b32 a29, 0
	v_accvgpr_write_b32 a30, 0
	v_accvgpr_write_b32 a31, 0
	s_mov_b32 s12, 0
	s_mov_b32 s13, 0
	v_mov_b32_e32 v9, v1
	v_mov_b32_e32 v11, v2
	v_xor_b32_e32 v10, 64, v1
	v_xor_b32_e32 v12, 64, v2
	s_waitcnt vmcnt(18)
	s_barrier
	ds_read_b128 v[16:19], v11
	ds_read_b128 v[24:27], v9
	ds_read_b128 v[20:23], v11 offset:2048
	ds_read_b128 v[28:31], v9 offset:2048
	ds_read_b128 v[32:35], v9 offset:4096
	ds_read_b128 v[36:39], v9 offset:6144
	s_add_i32 s23, s13, 0x6000
	s_cmp_lg_u32 s23, 0x18000
	s_cselect_b32 s23, s23, 0
	s_waitcnt lgkmcnt(0)
	v_mfma_f32_16x16x32_f16 a[0:3], v[16:19], v[24:27], a[0:3]
	ds_read_b128 v[40:43], v12
	v_mfma_f32_16x16x32_f16 a[4:7], v[20:23], v[24:27], a[4:7]
	ds_read_b128 v[48:51], v10
	v_mfma_f32_16x16x32_f16 a[8:11], v[16:19], v[28:31], a[8:11]
	ds_read_b128 v[44:47], v12 offset:2048
	v_mfma_f32_16x16x32_f16 a[12:15], v[20:23], v[28:31], a[12:15]
	ds_read_b128 v[52:55], v10 offset:2048
	v_mfma_f32_16x16x32_f16 a[16:19], v[16:19], v[32:35], a[16:19]
	ds_read_b128 v[56:59], v10 offset:4096
	v_mfma_f32_16x16x32_f16 a[20:23], v[20:23], v[32:35], a[20:23]
	ds_read_b128 v[60:63], v10 offset:6144
	v_mfma_f32_16x16x32_f16 a[24:27], v[16:19], v[36:39], a[24:27]
	v_add_u32_e32 v9, s23, v1
	v_add_u32_e32 v11, s23, v2
	v_mfma_f32_16x16x32_f16 a[28:31], v[20:23], v[36:39], a[28:31]
	v_xor_b32_e32 v10, 64, v9
	v_xor_b32_e32 v12, 64, v11
	s_waitcnt vmcnt(12)
	s_waitcnt lgkmcnt(0)
	s_barrier
	s_add_i32 s22, s12, 4
	s_lshl_b32 s22, s22, 7
	s_add_u32 s14, s4, s22
	s_addc_u32 s15, s5, 0
	s_add_u32 s16, s6, s22
	s_addc_u32 s17, s7, 0
	s_add_i32 s21, s13, s20
	v_mfma_f32_16x16x32_f16 a[0:3], v[40:43], v[48:51], a[0:3]
	ds_read_b128 v[16:19], v11
	v_mfma_f32_16x16x32_f16 a[4:7], v[44:47], v[48:51], a[4:7]
	ds_read_b128 v[24:27], v9
	s_mov_b32 m0, s21
	s_add_i32 s21, s21, 0x1000
	global_load_lds_dwordx4 v3, s[14:15]
	v_mfma_f32_16x16x32_f16 a[8:11], v[40:43], v[52:55], a[8:11]
	ds_read_b128 v[20:23], v11 offset:2048
	v_mfma_f32_16x16x32_f16 a[12:15], v[44:47], v[52:55], a[12:15]
	ds_read_b128 v[28:31], v9 offset:2048
	s_mov_b32 m0, s21
	s_add_i32 s21, s21, 0x1000
	global_load_lds_dwordx4 v4, s[14:15]
	v_mfma_f32_16x16x32_f16 a[16:19], v[40:43], v[56:59], a[16:19]
	ds_read_b128 v[32:35], v9 offset:4096
	v_mfma_f32_16x16x32_f16 a[20:23], v[44:47], v[56:59], a[20:23]
	ds_read_b128 v[36:39], v9 offset:6144
	s_mov_b32 m0, s21
	s_add_i32 s21, s21, 0x1000
	global_load_lds_dwordx4 v5, s[14:15]
	v_mfma_f32_16x16x32_f16 a[24:27], v[40:43], v[60:63], a[24:27]
	v_mfma_f32_16x16x32_f16 a[28:31], v[44:47], v[60:63], a[28:31]
	s_mov_b32 m0, s21
	s_add_i32 s21, s21, 0x1000
	global_load_lds_dwordx4 v6, s[14:15]
	s_mov_b32 s13, s23
	s_add_i32 s12, s12, 1
.Lg2_loop:
	s_add_i32 s23, s13, 0x6000
	s_cmp_lg_u32 s23, 0x18000
	s_cselect_b32 s23, s23, 0
	s_waitcnt lgkmcnt(0)
	v_mfma_f32_16x16x32_f16 a[0:3], v[16:19], v[24:27], a[0:3]
	ds_read_b128 v[40:43], v12
	v_mfma_f32_16x16x32_f16 a[4:7], v[20:23], v[24:27], a[4:7]
	ds_read_b128 v[48:51], v10
	v_mfma_f32_16x16x32_f16 a[8:11], v[16:19], v[28:31], a[8:11]
	ds_read_b128 v[44:47], v12 offset:2048
	v_mfma_f32_16x16x32_f16 a[12:15], v[20:23], v[28:31], a[12:15]
	ds_read_b128 v[52:55], v10 offset:2048
	s_mov_b32 m0, s21
	s_add_i32 s21, s21, 0x1000
	global_load_lds_dwordx4 v7, s[16:17]
	v_mfma_f32_16x16x32_f16 a[16:19], v[16:19], v[32:35], a[16:19]
	ds_read_b128 v[56:59], v10 offset:4096
	v_mfma_f32_16x16x32_f16 a[20:23], v[20:23], v[32:35], a[20:23]
	ds_read_b128 v[60:63], v10 offset:6144
	v_mfma_f32_16x16x32_f16 a[24:27], v[16:19], v[36:39], a[24:27]
	v_add_u32_e32 v9, s23, v1
	v_add_u32_e32 v11, s23, v2
	s_mov_b32 m0, s21
	s_nop 0
	global_load_lds_dwordx4 v8, s[16:17]
	v_mfma_f32_16x16x32_f16 a[28:31], v[20:23], v[36:39], a[28:31]
	v_xor_b32_e32 v10, 64, v9
	v_xor_b32_e32 v12, 64, v11
	s_waitcnt vmcnt(12)
	s_waitcnt lgkmcnt(0)
	s_barrier
	s_add_i32 s22, s12, 4
	s_lshl_b32 s22, s22, 7
	s_add_u32 s14, s4, s22
	s_addc_u32 s15, s5, 0
	s_add_u32 s16, s6, s22
	s_addc_u32 s17, s7, 0
	s_add_i32 s21, s13, s20
	v_mfma_f32_16x16x32_f16 a[0:3], v[40:43], v[48:51], a[0:3]
	ds_read_b128 v[16:19], v11
	v_mfma_f32_16x16x32_f16 a[4:7], v[44:47], v[48:51], a[4:7]
	ds_read_b128 v[24:27], v9
	s_mov_b32 m0, s21
	s_add_i32 s21, s21, 0x1000
	global_load_lds_dwordx4 v3, s[14:15]
	v_mfma_f32_16x16x32_f16 a[8:11], v[40:43], v[52:55], a[8:11]
	ds_read_b128 v[20:23], v11 offset:2048
	v_mfma_f32_16x16x32_f16 a[12:15], v[44:47], v[52:55], a[12:15]
	ds_read_b128 v[28:31], v9 offset:2048
	s_mov_b32 m0, s21
	s_add_i32 s21, s21, 0x1000
	global_load_lds_dwordx4 v4, s[14:15]
	v_mfma_f32_16x16x32_f16 a[16:19], v[40:43], v[56:59], a[16:19]
	ds_read_b128 v[32:35], v9 offset:4096
	v_mfma_f32_16x16x32_f16 a[20:23], v[44:47], v[56:59], a[20:23]
	ds_read_b128 v[36:39], v9 offset:6144
	s_mov_b32 m0, s21
	s_add_i32 s21, s21, 0x1000
	global_load_lds_dwordx4 v5, s[14:15]
	v_mfma_f32_16x16x32_f16 a[24:27], v[40:43], v[60:63], a[24:27]
	v_mfma_f32_16x16x32_f16 a[28:31], v[44:47], v[60:63], a[28:31]
	s_mov_b32 m0, s21
	s_add_i32 s21, s21, 0x1000
	global_load_lds_dwordx4 v6, s[14:15]
	s_mov_b32 s13, s23
	s_add_i32 s12, s12, 1
	s_cmp_lt_u32 s12, 20
	s_cbranch_scc1 .Lg2_loop
	s_add_i32 s23, s13, 0x6000
	s_cmp_lg_u32 s23, 0x18000
	s_cselect_b32 s23, s23, 0
	s_waitcnt lgkmcnt(0)
	v_mfma_f32_16x16x32_f16 a[0:3], v[16:19], v[24:27], a[0:3]
	ds_read_b128 v[40:43], v12
	v_mfma_f32_16x16x32_f16 a[4:7], v[20:23], v[24:27], a[4:7]
	ds_read_b128 v[48:51], v10
	v_mfma_f32_16x16x32_f16 a[8:11], v[16:19], v[28:31], a[8:11]
	ds_read_b128 v[44:47], v12 offset:2048
	v_mfma_f32_16x16x32_f16 a[12:15], v[20:23], v[28:31], a[12:15]
	ds_read_b128 v[52:55], v10 offset:2048
	s_mov_b32 m0, s21
	s_add_i32 s21, s21, 0x1000
	global_load_lds_dwordx4 v7, s[16:17]
	v_mfma_f32_16x16x32_f16 a[16:19], v[16:19], v[32:35], a[16:19]
	ds_read_b128 v[56:59], v10 offset:4096
	v_mfma_f32_16x16x32_f16 a[20:23], v[20:23], v[32:35], a[20:23]
	ds_read_b128 v[60:63], v10 offset:6144
	v_mfma_f32_16x16x32_f16 a[24:27], v[16:19], v[36:39], a[24:27]
	v_add_u32_e32 v9, s23, v1
	v_add_u32_e32 v11, s23, v2
	s_mov_b32 m0, s21
	s_nop 0
	global_load_lds_dwordx4 v8, s[16:17]
	v_mfma_f32_16x16x32_f16 a[28:31], v[20:23], v[36:39], a[28:31]
	v_xor_b32_e32 v10, 64, v9
	v_xor_b32_e32 v12, 64, v11
	s_waitcnt vmcnt(12)
	s_waitcnt lgkmcnt(0)
	s_barrier
	v_mfma_f32_16x16x32_f16 a[0:3], v[40:43], v[48:51], a[0:3]
	ds_read_b128 v[16:19], v11
	v_mfma_f32_16x16x32_f16 a[4:7], v[44:47], v[48:51], a[4:7]
	ds_read_b128 v[24:27], v9
	v_mfma_f32_16x16x32_f16 a[8:11], v[40:43], v[52:55], a[8:11]
	ds_read_b128 v[20:23], v11 offset:2048
	v_mfma_f32_16x16x32_f16 a[12:15], v[44:47], v[52:55], a[12:15]
	ds_read_b128 v[28:31], v9 offset:2048
	v_mfma_f32_16x16x32_f16 a[16:19], v[40:43], v[56:59], a[16:19]
	ds_read_b128 v[32:35], v9 offset:4096
	v_mfma_f32_16x16x32_f16 a[20:23], v[44:47], v[56:59], a[20:23]
	ds_read_b128 v[36:39], v9 offset:6144
	v_mfma_f32_16x16x32_f16 a[24:27], v[40:43], v[60:63], a[24:27]
	v_mfma_f32_16x16x32_f16 a[28:31], v[44:47], v[60:63], a[28:31]
	s_mov_b32 s13, s23
	s_add_i32 s12, s12, 1
	s_add_i32 s23, s13, 0x6000
	s_cmp_lg_u32 s23, 0x18000
	s_cselect_b32 s23, s23, 0
	s_waitcnt lgkmcnt(0)
	v_mfma_f32_16x16x32_f16 a[0:3], v[16:19], v[24:27], a[0:3]
	ds_read_b128 v[40:43], v12
	v_mfma_f32_16x16x32_f16 a[4:7], v[20:23], v[24:27], a[4:7]
	ds_read_b128 v[48:51], v10
	v_mfma_f32_16x16x32_f16 a[8:11], v[16:19], v[28:31], a[8:11]
	ds_read_b128 v[44:47], v12 offset:2048
	v_mfma_f32_16x16x32_f16 a[12:15], v[20:23], v[28:31], a[12:15]
	ds_read_b128 v[52:55], v10 offset:2048
	v_mfma_f32_16x16x32_f16 a[16:19], v[16:19], v[32:35], a[16:19]
	ds_read_b128 v[56:59], v10 offset:4096
	v_mfma_f32_16x16x32_f16 a[20:23], v[20:23], v[32:35], a[20:23]
	ds_read_b128 v[60:63], v10 offset:6144
	v_mfma_f32_16x16x32_f16 a[24:27], v[16:19], v[36:39], a[24:27]
	v_add_u32_e32 v9, s23, v1
	v_add_u32_e32 v11, s23, v2
	v_mfma_f32_16x16x32_f16 a[28:31], v[20:23], v[36:39], a[28:31]
	v_xor_b32_e32 v10, 64, v9
	v_xor_b32_e32 v12, 64, v11
	s_waitcnt vmcnt(6)
	s_waitcnt lgkmcnt(0)
	s_barrier
	v_mfma_f32_16x16x32_f16 a[0:3], v[40:43], v[48:51], a[0:3]
	ds_read_b128 v[16:19], v11
	v_mfma_f32_16x16x32_f16 a[4:7], v[44:47], v[48:51], a[4:7]
	ds_read_b128 v[24:27], v9
	v_mfma_f32_16x16x32_f16 a[8:11], v[40:43], v[52:55], a[8:11]
	ds_read_b128 v[20:23], v11 offset:2048
	v_mfma_f32_16x16x32_f16 a[12:15], v[44:47], v[52:55], a[12:15]
	ds_read_b128 v[28:31], v9 offset:2048
	v_mfma_f32_16x16x32_f16 a[16:19], v[40:43], v[56:59], a[16:19]
	ds_read_b128 v[32:35], v9 offset:4096
	v_mfma_f32_16x16x32_f16 a[20:23], v[44:47], v[56:59], a[20:23]
	ds_read_b128 v[36:39], v9 offset:6144
	v_mfma_f32_16x16x32_f16 a[24:27], v[40:43], v[60:63], a[24:27]
	v_mfma_f32_16x16x32_f16 a[28:31], v[44:47], v[60:63], a[28:31]
	s_mov_b32 s13, s23
	s_add_i32 s12, s12, 1
	s_add_i32 s23, s13, 0x6000
	s_cmp_lg_u32 s23, 0x18000
	s_cselect_b32 s23, s23, 0
	s_waitcnt lgkmcnt(0)
	v_mfma_f32_16x16x32_f16 a[0:3], v[16:19], v[24:27], a[0:3]
	ds_read_b128 v[40:43], v12
	v_mfma_f32_16x16x32_f16 a[4:7], v[20:23], v[24:27], a[4:7]
	ds_read_b128 v[48:51], v10
	v_mfma_f32_16x16x32_f16 a[8:11], v[16:19], v[28:31], a[8:11]
	ds_read_b128 v[44:47], v12 offset:2048
	v_mfma_f32_16x16x32_f16 a[12:15], v[20:23], v[28:31], a[12:15]
	ds_read_b128 v[52:55], v10 offset:2048
	v_mfma_f32_16x16x32_f16 a[16:19], v[16:19], v[32:35], a[16:19]
	ds_read_b128 v[56:59], v10 offset:4096
	v_mfma_f32_16x16x32_f16 a[20:23], v[20:23], v[32:35], a[20:23]
	ds_read_b128 v[60:63], v10 offset:6144
	v_mfma_f32_16x16x32_f16 a[24:27], v[16:19], v[36:39], a[24:27]
	v_add_u32_e32 v9, s23, v1
	v_add_u32_e32 v11, s23, v2
	v_mfma_f32_16x16x32_f16 a[28:31], v[20:23], v[36:39], a[28:31]
	v_xor_b32_e32 v10, 64, v9
	v_xor_b32_e32 v12, 64, v11
	s_waitcnt vmcnt(0)
	s_waitcnt lgkmcnt(0)
	s_barrier
	v_mfma_f32_16x16x32_f16 a[0:3], v[40:43], v[48:51], a[0:3]
	ds_read_b128 v[16:19], v11
	v_mfma_f32_16x16x32_f16 a[4:7], v[44:47], v[48:51], a[4:7]
	ds_read_b128 v[24:27], v9
	v_mfma_f32_16x16x32_f16 a[8:11], v[40:43], v[52:55], a[8:11]
	ds_read_b128 v[20:23], v11 offset:2048
	v_mfma_f32_16x16x32_f16 a[12:15], v[44:47], v[52:55], a[12:15]
	ds_read_b128 v[28:31], v9 offset:2048
	v_mfma_f32_16x16x32_f16 a[16:19], v[40:43], v[56:59], a[16:19]
	ds_read_b128 v[32:35], v9 offset:4096
	v_mfma_f32_16x16x32_f16 a[20:23], v[44:47], v[56:59], a[20:23]
	ds_read_b128 v[36:39], v9 offset:6144
	v_mfma_f32_16x16x32_f16 a[24:27], v[40:43], v[60:63], a[24:27]
	v_mfma_f32_16x16x32_f16 a[28:31], v[44:47], v[60:63], a[28:31]
	s_mov_b32 s13, s23
	s_add_i32 s12, s12, 1
	s_add_i32 s23, s13, 0x6000
	s_cmp_lg_u32 s23, 0x18000
	s_cselect_b32 s23, s23, 0
	s_waitcnt lgkmcnt(0)
	v_mfma_f32_16x16x32_f16 a[0:3], v[16:19], v[24:27], a[0:3]
	ds_read_b128 v[40:43], v12
	v_mfma_f32_16x16x32_f16 a[4:7], v[20:23], v[24:27], a[4:7]
	ds_read_b128 v[48:51], v10
	v_mfma_f32_16x16x32_f16 a[8:11], v[16:19], v[28:31], a[8:11]
	ds_read_b128 v[44:47], v12 offset:2048
	v_mfma_f32_16x16x32_f16 a[12:15], v[20:23], v[28:31], a[12:15]
	ds_read_b128 v[52:55], v10 offset:2048
	v_mfma_f32_16x16x32_f16 a[16:19], v[16:19], v[32:35], a[16:19]
	ds_read_b128 v[56:59], v10 offset:4096
	v_mfma_f32_16x16x32_f16 a[20:23], v[20:23], v[32:35], a[20:23]
	ds_read_b128 v[60:63], v10 offset:6144
	v_mfma_f32_16x16x32_f16 a[24:27], v[16:19], v[36:39], a[24:27]
	v_add_u32_e32 v9, s23, v1
	v_add_u32_e32 v11, s23, v2
	v_mfma_f32_16x16x32_f16 a[28:31], v[20:23], v[36:39], a[28:31]
	v_xor_b32_e32 v10, 64, v9
	v_xor_b32_e32 v12, 64, v11
	s_waitcnt lgkmcnt(0)
	s_barrier
	v_mfma_f32_16x16x32_f16 a[0:3], v[40:43], v[48:51], a[0:3]
	ds_read_b128 v[16:19], v11
	v_mfma_f32_16x16x32_f16 a[4:7], v[44:47], v[48:51], a[4:7]
	ds_read_b128 v[24:27], v9
	v_mfma_f32_16x16x32_f16 a[8:11], v[40:43], v[52:55], a[8:11]
	ds_read_b128 v[20:23], v11 offset:2048
	v_mfma_f32_16x16x32_f16 a[12:15], v[44:47], v[52:55], a[12:15]
	ds_read_b128 v[28:31], v9 offset:2048
	v_mfma_f32_16x16x32_f16 a[16:19], v[40:43], v[56:59], a[16:19]
	ds_read_b128 v[32:35], v9 offset:4096
	v_mfma_f32_16x16x32_f16 a[20:23], v[44:47], v[56:59], a[20:23]
	ds_read_b128 v[36:39], v9 offset:6144
	v_mfma_f32_16x16x32_f16 a[24:27], v[40:43], v[60:63], a[24:27]
	v_mfma_f32_16x16x32_f16 a[28:31], v[44:47], v[60:63], a[28:31]
	s_mov_b32 s13, s23
	s_add_i32 s12, s12, 1
	s_waitcnt vmcnt(0) lgkmcnt(0)
	v_and_b32_e32 v13, 15, v0
	v_lshrrev_b32_e32 v14, 7, v0
	v_lshl_add_u32 v13, v14, 6, v13
	v_add_u32_e32 v13, s10, v13
	v_bfe_u32 v14, v0, 6, 1
	v_bfe_u32 v15, v0, 4, 2
	v_lshlrev_b32_e32 v14, 5, v14
	v_lshl_add_u32 v14, v15, 2, v14
	v_add_u32_e32 v14, s11, v14
	v_lshlrev_b32_e32 v13, 10, v13
	v_add_u32_e32 v13, v13, v14
	v_lshlrev_b32_e32 v13, 2, v13
	v_add_u32_e32 v14, 0x10000, v13
	v_add_u32_e32 v15, 0x20000, v13
	v_add_u32_e32 v16, 0x30000, v13
	s_nop 7
	global_store_dwordx4 v13, a[0:3], s[8:9]
	global_store_dwordx4 v13, a[4:7], s[8:9] offset:64
	global_store_dwordx4 v14, a[8:11], s[8:9]
	global_store_dwordx4 v14, a[12:15], s[8:9] offset:64
	global_store_dwordx4 v15, a[16:19], s[8:9]
	global_store_dwordx4 v15, a[20:23], s[8:9] offset:64
	global_store_dwordx4 v16, a[24:27], s[8:9]
	global_store_dwordx4 v16, a[28:31], s[8:9] offset:64
	s_endpgm
	.p2alignl 8, 3212836864
